# ada modulation GEMV loop rewritten: 32 weight rows kept in flight per lane (rolling prefetch) instead of a drain every 16
# baseline (speedup 1.0000x reference)
; __device__ __forceinline__ void ada_phase(LAS unsigned char* lds, const float* __restrict__ cin, const float* __restrict__ w_ada, const float* __restrict__ b_ada, float* __restrict__ MOD, int G, int c) {
;     ...
;         if (tid < 384) {
;             const int cl = tid % 96, kp = tid / 96;
;             const float* w = w_ada + ((size_t)l * D + kp * 256) * 6 * D + j0 + cl;
;             float acc[NB];
; #pragma unroll
;             for (int b = 0; b < NB; ++b) acc[b] = 0.f;
; #pragma unroll 16
;             for (int k = 0; k < 256; ++k) {
;                 const float wv = w[(size_t)k * 6 * D];
; #pragma unroll
;                 for (int b = 0; b < NB; ++b) acc[b] += cond[b * D + kp * 256 + k] * wv;
;             }
; #pragma unroll
;             for (int b = 0; b < NB; ++b) part[(kp * 96 + cl) * 8 + b] = acc[b];
.LBB0_12:
	s_ashr_i32 s10, s21, 31
	s_lshr_b32 s10, s10, 26
	s_add_i32 s10, s21, s10
	s_ashr_i32 s18, s10, 6
	s_and_saveexec_b64 s[14:15], vcc
	s_cbranch_execz .LBB0_16
	s_mul_i32 s10, s18, 0x1800
	s_sub_i32 s10, s24, s10
	s_ashr_i32 s11, s10, 31
	s_mul_i32 s17, s18, 0x1800000
	s_lshl_b64 s[10:11], s[10:11], 2
	s_mul_hi_i32 s16, s18, 0x1800000
	s_add_u32 s10, s17, s10
	s_addc_u32 s11, s16, s11
	v_mov_b32_e32 v10, 0
	v_lshl_add_u64 v[8:9], v[6:7], 0, s[10:11]
	s_mov_b64 s[16:17], 0
	v_mov_b32_e32 v41, v1
	v_mov_b32_e32 v11, v10
	v_mov_b32_e32 v16, v10
	v_mov_b32_e32 v17, v10
	v_mov_b32_e32 v14, v10
	v_mov_b32_e32 v15, v10
	v_mov_b32_e32 v12, v10
	v_mov_b32_e32 v13, v10
	v_mov_b32_e32 v196, v8
	v_mov_b32_e32 v197, v9
	s_mov_b32 s16, 0x6000
	s_mov_b32 s17, 0
	global_load_dword v100, v[196:197], off
	v_lshl_add_u64 v[196:197], v[196:197], 0, s[16:17]
	global_load_dword v102, v[196:197], off
	v_lshl_add_u64 v[196:197], v[196:197], 0, s[16:17]
	global_load_dword v104, v[196:197], off
	v_lshl_add_u64 v[196:197], v[196:197], 0, s[16:17]
	global_load_dword v106, v[196:197], off
	v_lshl_add_u64 v[196:197], v[196:197], 0, s[16:17]
	global_load_dword v108, v[196:197], off
	v_lshl_add_u64 v[196:197], v[196:197], 0, s[16:17]
	global_load_dword v110, v[196:197], off
	v_lshl_add_u64 v[196:197], v[196:197], 0, s[16:17]
	global_load_dword v112, v[196:197], off
	v_lshl_add_u64 v[196:197], v[196:197], 0, s[16:17]
	global_load_dword v114, v[196:197], off
	v_lshl_add_u64 v[196:197], v[196:197], 0, s[16:17]
	global_load_dword v116, v[196:197], off
	v_lshl_add_u64 v[196:197], v[196:197], 0, s[16:17]
	global_load_dword v118, v[196:197], off
	v_lshl_add_u64 v[196:197], v[196:197], 0, s[16:17]
	global_load_dword v120, v[196:197], off
	v_lshl_add_u64 v[196:197], v[196:197], 0, s[16:17]
	global_load_dword v122, v[196:197], off
	v_lshl_add_u64 v[196:197], v[196:197], 0, s[16:17]
	global_load_dword v124, v[196:197], off
	v_lshl_add_u64 v[196:197], v[196:197], 0, s[16:17]
	global_load_dword v126, v[196:197], off
	v_lshl_add_u64 v[196:197], v[196:197], 0, s[16:17]
	global_load_dword v128, v[196:197], off
	v_lshl_add_u64 v[196:197], v[196:197], 0, s[16:17]
	global_load_dword v130, v[196:197], off
	v_lshl_add_u64 v[196:197], v[196:197], 0, s[16:17]
	global_load_dword v132, v[196:197], off
	v_lshl_add_u64 v[196:197], v[196:197], 0, s[16:17]
	global_load_dword v134, v[196:197], off
	v_lshl_add_u64 v[196:197], v[196:197], 0, s[16:17]
	global_load_dword v136, v[196:197], off
	v_lshl_add_u64 v[196:197], v[196:197], 0, s[16:17]
	global_load_dword v138, v[196:197], off
	v_lshl_add_u64 v[196:197], v[196:197], 0, s[16:17]
	global_load_dword v140, v[196:197], off
	v_lshl_add_u64 v[196:197], v[196:197], 0, s[16:17]
	global_load_dword v142, v[196:197], off
	v_lshl_add_u64 v[196:197], v[196:197], 0, s[16:17]
	global_load_dword v144, v[196:197], off
	v_lshl_add_u64 v[196:197], v[196:197], 0, s[16:17]
	global_load_dword v146, v[196:197], off
	v_lshl_add_u64 v[196:197], v[196:197], 0, s[16:17]
	global_load_dword v148, v[196:197], off
	v_lshl_add_u64 v[196:197], v[196:197], 0, s[16:17]
	global_load_dword v150, v[196:197], off
	v_lshl_add_u64 v[196:197], v[196:197], 0, s[16:17]
	global_load_dword v152, v[196:197], off
	v_lshl_add_u64 v[196:197], v[196:197], 0, s[16:17]
	global_load_dword v154, v[196:197], off
	v_lshl_add_u64 v[196:197], v[196:197], 0, s[16:17]
	global_load_dword v156, v[196:197], off
	v_lshl_add_u64 v[196:197], v[196:197], 0, s[16:17]
	global_load_dword v158, v[196:197], off
	v_lshl_add_u64 v[196:197], v[196:197], 0, s[16:17]
	global_load_dword v160, v[196:197], off
	v_lshl_add_u64 v[196:197], v[196:197], 0, s[16:17]
	global_load_dword v162, v[196:197], off
	v_lshl_add_u64 v[196:197], v[196:197], 0, s[16:17]
	v_mov_b32_e32 v198, v41
	ds_read2st64_b32 v[164:165], v198 offset0:0 offset1:16
	ds_read2st64_b32 v[166:167], v198 offset0:32 offset1:48
	ds_read2st64_b32 v[168:169], v198 offset0:64 offset1:80
	ds_read2st64_b32 v[170:171], v198 offset0:96 offset1:112
	v_add_u32_e32 v198, 4, v198
	ds_read2st64_b32 v[172:173], v198 offset0:0 offset1:16
	ds_read2st64_b32 v[174:175], v198 offset0:32 offset1:48
	ds_read2st64_b32 v[176:177], v198 offset0:64 offset1:80
	ds_read2st64_b32 v[178:179], v198 offset0:96 offset1:112
	v_add_u32_e32 v198, 4, v198
	ds_read2st64_b32 v[180:181], v198 offset0:0 offset1:16
	ds_read2st64_b32 v[182:183], v198 offset0:32 offset1:48
	ds_read2st64_b32 v[184:185], v198 offset0:64 offset1:80
	ds_read2st64_b32 v[186:187], v198 offset0:96 offset1:112
	v_add_u32_e32 v198, 4, v198
	s_mov_b32 s10, 7
.Lada_blk:
	s_cmp_lg_u32 s10, 0
	s_cbranch_scc1 .Lada_go
	v_mov_b32_e32 v196, v8
	v_mov_b32_e32 v197, v9
	s_mov_b32 s16, 0
; __device__ __forceinline__ void ada_phase(LAS unsigned char* lds, const float* __restrict__ cin, const float* __restrict__ w_ada, const float* __restrict__ b_ada, float* __restrict__ MOD, int G, int c) {
;     ...
; #pragma unroll 16
;             for (int k = 0; k < 256; ++k) {
;                 const float wv = w[(size_t)k * 6 * D];
; #pragma unroll
;                 for (int b = 0; b < NB; ++b) acc[b] += cond[b * D + kp * 256 + k] * wv;
;             }
.Lada_go:
	ds_read2st64_b32 v[188:189], v198 offset0:0 offset1:16
	ds_read2st64_b32 v[190:191], v198 offset0:32 offset1:48
	ds_read2st64_b32 v[192:193], v198 offset0:64 offset1:80
	ds_read2st64_b32 v[194:195], v198 offset0:96 offset1:112
	v_add_u32_e32 v198, 4, v198
	s_waitcnt vmcnt(31) lgkmcnt(12)
	v_pk_fma_f32 v[16:17], v[100:101], v[164:165], v[16:17] op_sel_hi:[0,1,1]
	v_pk_fma_f32 v[14:15], v[100:101], v[166:167], v[14:15] op_sel_hi:[0,1,1]
	v_pk_fma_f32 v[12:13], v[100:101], v[168:169], v[12:13] op_sel_hi:[0,1,1]
	v_pk_fma_f32 v[10:11], v[100:101], v[170:171], v[10:11] op_sel_hi:[0,1,1]
	global_load_dword v100, v[196:197], off
	v_lshl_add_u64 v[196:197], v[196:197], 0, s[16:17]
	ds_read2st64_b32 v[164:165], v198 offset0:0 offset1:16
	ds_read2st64_b32 v[166:167], v198 offset0:32 offset1:48
	ds_read2st64_b32 v[168:169], v198 offset0:64 offset1:80
	ds_read2st64_b32 v[170:171], v198 offset0:96 offset1:112
	v_add_u32_e32 v198, 4, v198
	s_waitcnt vmcnt(31) lgkmcnt(12)
	v_pk_fma_f32 v[16:17], v[102:103], v[172:173], v[16:17] op_sel_hi:[0,1,1]
	v_pk_fma_f32 v[14:15], v[102:103], v[174:175], v[14:15] op_sel_hi:[0,1,1]
	v_pk_fma_f32 v[12:13], v[102:103], v[176:177], v[12:13] op_sel_hi:[0,1,1]
	v_pk_fma_f32 v[10:11], v[102:103], v[178:179], v[10:11] op_sel_hi:[0,1,1]
	global_load_dword v102, v[196:197], off
	v_lshl_add_u64 v[196:197], v[196:197], 0, s[16:17]
	ds_read2st64_b32 v[172:173], v198 offset0:0 offset1:16
	ds_read2st64_b32 v[174:175], v198 offset0:32 offset1:48
	ds_read2st64_b32 v[176:177], v198 offset0:64 offset1:80
	ds_read2st64_b32 v[178:179], v198 offset0:96 offset1:112
	v_add_u32_e32 v198, 4, v198
	s_waitcnt vmcnt(31) lgkmcnt(12)
	v_pk_fma_f32 v[16:17], v[104:105], v[180:181], v[16:17] op_sel_hi:[0,1,1]
	v_pk_fma_f32 v[14:15], v[104:105], v[182:183], v[14:15] op_sel_hi:[0,1,1]
	v_pk_fma_f32 v[12:13], v[104:105], v[184:185], v[12:13] op_sel_hi:[0,1,1]
	v_pk_fma_f32 v[10:11], v[104:105], v[186:187], v[10:11] op_sel_hi:[0,1,1]
	global_load_dword v104, v[196:197], off
	v_lshl_add_u64 v[196:197], v[196:197], 0, s[16:17]
	ds_read2st64_b32 v[180:181], v198 offset0:0 offset1:16
	ds_read2st64_b32 v[182:183], v198 offset0:32 offset1:48
	ds_read2st64_b32 v[184:185], v198 offset0:64 offset1:80
	ds_read2st64_b32 v[186:187], v198 offset0:96 offset1:112
	v_add_u32_e32 v198, 4, v198
	s_waitcnt vmcnt(31) lgkmcnt(12)
	v_pk_fma_f32 v[16:17], v[106:107], v[188:189], v[16:17] op_sel_hi:[0,1,1]
	v_pk_fma_f32 v[14:15], v[106:107], v[190:191], v[14:15] op_sel_hi:[0,1,1]
	v_pk_fma_f32 v[12:13], v[106:107], v[192:193], v[12:13] op_sel_hi:[0,1,1]
	v_pk_fma_f32 v[10:11], v[106:107], v[194:195], v[10:11] op_sel_hi:[0,1,1]
	global_load_dword v106, v[196:197], off
	v_lshl_add_u64 v[196:197], v[196:197], 0, s[16:17]
	ds_read2st64_b32 v[188:189], v198 offset0:0 offset1:16
	ds_read2st64_b32 v[190:191], v198 offset0:32 offset1:48
	ds_read2st64_b32 v[192:193], v198 offset0:64 offset1:80
	ds_read2st64_b32 v[194:195], v198 offset0:96 offset1:112
	v_add_u32_e32 v198, 4, v198
	s_waitcnt vmcnt(31) lgkmcnt(12)
	v_pk_fma_f32 v[16:17], v[108:109], v[164:165], v[16:17] op_sel_hi:[0,1,1]
	v_pk_fma_f32 v[14:15], v[108:109], v[166:167], v[14:15] op_sel_hi:[0,1,1]
	v_pk_fma_f32 v[12:13], v[108:109], v[168:169], v[12:13] op_sel_hi:[0,1,1]
	v_pk_fma_f32 v[10:11], v[108:109], v[170:171], v[10:11] op_sel_hi:[0,1,1]
	global_load_dword v108, v[196:197], off
	v_lshl_add_u64 v[196:197], v[196:197], 0, s[16:17]
	ds_read2st64_b32 v[164:165], v198 offset0:0 offset1:16
	ds_read2st64_b32 v[166:167], v198 offset0:32 offset1:48
	ds_read2st64_b32 v[168:169], v198 offset0:64 offset1:80
	ds_read2st64_b32 v[170:171], v198 offset0:96 offset1:112
	v_add_u32_e32 v198, 4, v198
	s_waitcnt vmcnt(31) lgkmcnt(12)
	v_pk_fma_f32 v[16:17], v[110:111], v[172:173], v[16:17] op_sel_hi:[0,1,1]
	v_pk_fma_f32 v[14:15], v[110:111], v[174:175], v[14:15] op_sel_hi:[0,1,1]
	v_pk_fma_f32 v[12:13], v[110:111], v[176:177], v[12:13] op_sel_hi:[0,1,1]
	v_pk_fma_f32 v[10:11], v[110:111], v[178:179], v[10:11] op_sel_hi:[0,1,1]
	global_load_dword v110, v[196:197], off
	v_lshl_add_u64 v[196:197], v[196:197], 0, s[16:17]
	ds_read2st64_b32 v[172:173], v198 offset0:0 offset1:16
	ds_read2st64_b32 v[174:175], v198 offset0:32 offset1:48
	ds_read2st64_b32 v[176:177], v198 offset0:64 offset1:80
	ds_read2st64_b32 v[178:179], v198 offset0:96 offset1:112
	v_add_u32_e32 v198, 4, v198
	s_waitcnt vmcnt(31) lgkmcnt(12)
	v_pk_fma_f32 v[16:17], v[112:113], v[180:181], v[16:17] op_sel_hi:[0,1,1]
	v_pk_fma_f32 v[14:15], v[112:113], v[182:183], v[14:15] op_sel_hi:[0,1,1]
	v_pk_fma_f32 v[12:13], v[112:113], v[184:185], v[12:13] op_sel_hi:[0,1,1]
	v_pk_fma_f32 v[10:11], v[112:113], v[186:187], v[10:11] op_sel_hi:[0,1,1]
	global_load_dword v112, v[196:197], off
	v_lshl_add_u64 v[196:197], v[196:197], 0, s[16:17]
	ds_read2st64_b32 v[180:181], v198 offset0:0 offset1:16
	ds_read2st64_b32 v[182:183], v198 offset0:32 offset1:48
	ds_read2st64_b32 v[184:185], v198 offset0:64 offset1:80
	ds_read2st64_b32 v[186:187], v198 offset0:96 offset1:112
	v_add_u32_e32 v198, 4, v198
	s_waitcnt vmcnt(31) lgkmcnt(12)
	v_pk_fma_f32 v[16:17], v[114:115], v[188:189], v[16:17] op_sel_hi:[0,1,1]
	v_pk_fma_f32 v[14:15], v[114:115], v[190:191], v[14:15] op_sel_hi:[0,1,1]
	v_pk_fma_f32 v[12:13], v[114:115], v[192:193], v[12:13] op_sel_hi:[0,1,1]
	v_pk_fma_f32 v[10:11], v[114:115], v[194:195], v[10:11] op_sel_hi:[0,1,1]
	global_load_dword v114, v[196:197], off
	v_lshl_add_u64 v[196:197], v[196:197], 0, s[16:17]
	ds_read2st64_b32 v[188:189], v198 offset0:0 offset1:16
	ds_read2st64_b32 v[190:191], v198 offset0:32 offset1:48
	ds_read2st64_b32 v[192:193], v198 offset0:64 offset1:80
	ds_read2st64_b32 v[194:195], v198 offset0:96 offset1:112
	v_add_u32_e32 v198, 4, v198
	s_waitcnt vmcnt(31) lgkmcnt(12)
; __device__ __forceinline__ void ada_phase(LAS unsigned char* lds, const float* __restrict__ cin, const float* __restrict__ w_ada, const float* __restrict__ b_ada, float* __restrict__ MOD, int G, int c) {
;     ...
; #pragma unroll 16
;             for (int k = 0; k < 256; ++k) {
;                 const float wv = w[(size_t)k * 6 * D];
; #pragma unroll
;                 for (int b = 0; b < NB; ++b) acc[b] += cond[b * D + kp * 256 + k] * wv;
;             }
	v_pk_fma_f32 v[16:17], v[116:117], v[164:165], v[16:17] op_sel_hi:[0,1,1]
	v_pk_fma_f32 v[14:15], v[116:117], v[166:167], v[14:15] op_sel_hi:[0,1,1]
	v_pk_fma_f32 v[12:13], v[116:117], v[168:169], v[12:13] op_sel_hi:[0,1,1]
	v_pk_fma_f32 v[10:11], v[116:117], v[170:171], v[10:11] op_sel_hi:[0,1,1]
	global_load_dword v116, v[196:197], off
	v_lshl_add_u64 v[196:197], v[196:197], 0, s[16:17]
	ds_read2st64_b32 v[164:165], v198 offset0:0 offset1:16
	ds_read2st64_b32 v[166:167], v198 offset0:32 offset1:48
	ds_read2st64_b32 v[168:169], v198 offset0:64 offset1:80
	ds_read2st64_b32 v[170:171], v198 offset0:96 offset1:112
	v_add_u32_e32 v198, 4, v198
	s_waitcnt vmcnt(31) lgkmcnt(12)
	v_pk_fma_f32 v[16:17], v[118:119], v[172:173], v[16:17] op_sel_hi:[0,1,1]
	v_pk_fma_f32 v[14:15], v[118:119], v[174:175], v[14:15] op_sel_hi:[0,1,1]
	v_pk_fma_f32 v[12:13], v[118:119], v[176:177], v[12:13] op_sel_hi:[0,1,1]
	v_pk_fma_f32 v[10:11], v[118:119], v[178:179], v[10:11] op_sel_hi:[0,1,1]
	global_load_dword v118, v[196:197], off
	v_lshl_add_u64 v[196:197], v[196:197], 0, s[16:17]
	ds_read2st64_b32 v[172:173], v198 offset0:0 offset1:16
	ds_read2st64_b32 v[174:175], v198 offset0:32 offset1:48
	ds_read2st64_b32 v[176:177], v198 offset0:64 offset1:80
	ds_read2st64_b32 v[178:179], v198 offset0:96 offset1:112
	v_add_u32_e32 v198, 4, v198
	s_waitcnt vmcnt(31) lgkmcnt(12)
	v_pk_fma_f32 v[16:17], v[120:121], v[180:181], v[16:17] op_sel_hi:[0,1,1]
	v_pk_fma_f32 v[14:15], v[120:121], v[182:183], v[14:15] op_sel_hi:[0,1,1]
	v_pk_fma_f32 v[12:13], v[120:121], v[184:185], v[12:13] op_sel_hi:[0,1,1]
	v_pk_fma_f32 v[10:11], v[120:121], v[186:187], v[10:11] op_sel_hi:[0,1,1]
	global_load_dword v120, v[196:197], off
	v_lshl_add_u64 v[196:197], v[196:197], 0, s[16:17]
	ds_read2st64_b32 v[180:181], v198 offset0:0 offset1:16
	ds_read2st64_b32 v[182:183], v198 offset0:32 offset1:48
	ds_read2st64_b32 v[184:185], v198 offset0:64 offset1:80
	ds_read2st64_b32 v[186:187], v198 offset0:96 offset1:112
	v_add_u32_e32 v198, 4, v198
	s_waitcnt vmcnt(31) lgkmcnt(12)
	v_pk_fma_f32 v[16:17], v[122:123], v[188:189], v[16:17] op_sel_hi:[0,1,1]
	v_pk_fma_f32 v[14:15], v[122:123], v[190:191], v[14:15] op_sel_hi:[0,1,1]
	v_pk_fma_f32 v[12:13], v[122:123], v[192:193], v[12:13] op_sel_hi:[0,1,1]
	v_pk_fma_f32 v[10:11], v[122:123], v[194:195], v[10:11] op_sel_hi:[0,1,1]
	global_load_dword v122, v[196:197], off
	v_lshl_add_u64 v[196:197], v[196:197], 0, s[16:17]
	ds_read2st64_b32 v[188:189], v198 offset0:0 offset1:16
	ds_read2st64_b32 v[190:191], v198 offset0:32 offset1:48
	ds_read2st64_b32 v[192:193], v198 offset0:64 offset1:80
	ds_read2st64_b32 v[194:195], v198 offset0:96 offset1:112
	v_add_u32_e32 v198, 4, v198
	s_waitcnt vmcnt(31) lgkmcnt(12)
	v_pk_fma_f32 v[16:17], v[124:125], v[164:165], v[16:17] op_sel_hi:[0,1,1]
	v_pk_fma_f32 v[14:15], v[124:125], v[166:167], v[14:15] op_sel_hi:[0,1,1]
	v_pk_fma_f32 v[12:13], v[124:125], v[168:169], v[12:13] op_sel_hi:[0,1,1]
	v_pk_fma_f32 v[10:11], v[124:125], v[170:171], v[10:11] op_sel_hi:[0,1,1]
	global_load_dword v124, v[196:197], off
	v_lshl_add_u64 v[196:197], v[196:197], 0, s[16:17]
	ds_read2st64_b32 v[164:165], v198 offset0:0 offset1:16
	ds_read2st64_b32 v[166:167], v198 offset0:32 offset1:48
	ds_read2st64_b32 v[168:169], v198 offset0:64 offset1:80
	ds_read2st64_b32 v[170:171], v198 offset0:96 offset1:112
	v_add_u32_e32 v198, 4, v198
	s_waitcnt vmcnt(31) lgkmcnt(12)
	v_pk_fma_f32 v[16:17], v[126:127], v[172:173], v[16:17] op_sel_hi:[0,1,1]
	v_pk_fma_f32 v[14:15], v[126:127], v[174:175], v[14:15] op_sel_hi:[0,1,1]
	v_pk_fma_f32 v[12:13], v[126:127], v[176:177], v[12:13] op_sel_hi:[0,1,1]
	v_pk_fma_f32 v[10:11], v[126:127], v[178:179], v[10:11] op_sel_hi:[0,1,1]
	global_load_dword v126, v[196:197], off
	v_lshl_add_u64 v[196:197], v[196:197], 0, s[16:17]
	ds_read2st64_b32 v[172:173], v198 offset0:0 offset1:16
	ds_read2st64_b32 v[174:175], v198 offset0:32 offset1:48
	ds_read2st64_b32 v[176:177], v198 offset0:64 offset1:80
	ds_read2st64_b32 v[178:179], v198 offset0:96 offset1:112
	v_add_u32_e32 v198, 4, v198
	s_waitcnt vmcnt(31) lgkmcnt(12)
	v_pk_fma_f32 v[16:17], v[128:129], v[180:181], v[16:17] op_sel_hi:[0,1,1]
	v_pk_fma_f32 v[14:15], v[128:129], v[182:183], v[14:15] op_sel_hi:[0,1,1]
	v_pk_fma_f32 v[12:13], v[128:129], v[184:185], v[12:13] op_sel_hi:[0,1,1]
	v_pk_fma_f32 v[10:11], v[128:129], v[186:187], v[10:11] op_sel_hi:[0,1,1]
	global_load_dword v128, v[196:197], off
	v_lshl_add_u64 v[196:197], v[196:197], 0, s[16:17]
	ds_read2st64_b32 v[180:181], v198 offset0:0 offset1:16
	ds_read2st64_b32 v[182:183], v198 offset0:32 offset1:48
	ds_read2st64_b32 v[184:185], v198 offset0:64 offset1:80
	ds_read2st64_b32 v[186:187], v198 offset0:96 offset1:112
	v_add_u32_e32 v198, 4, v198
	s_waitcnt vmcnt(31) lgkmcnt(12)
	v_pk_fma_f32 v[16:17], v[130:131], v[188:189], v[16:17] op_sel_hi:[0,1,1]
	v_pk_fma_f32 v[14:15], v[130:131], v[190:191], v[14:15] op_sel_hi:[0,1,1]
	v_pk_fma_f32 v[12:13], v[130:131], v[192:193], v[12:13] op_sel_hi:[0,1,1]
	v_pk_fma_f32 v[10:11], v[130:131], v[194:195], v[10:11] op_sel_hi:[0,1,1]
	global_load_dword v130, v[196:197], off
	v_lshl_add_u64 v[196:197], v[196:197], 0, s[16:17]
	ds_read2st64_b32 v[188:189], v198 offset0:0 offset1:16
	ds_read2st64_b32 v[190:191], v198 offset0:32 offset1:48
	ds_read2st64_b32 v[192:193], v198 offset0:64 offset1:80
	ds_read2st64_b32 v[194:195], v198 offset0:96 offset1:112
	v_add_u32_e32 v198, 4, v198
	s_waitcnt vmcnt(31) lgkmcnt(12)
; __device__ __forceinline__ void ada_phase(LAS unsigned char* lds, const float* __restrict__ cin, const float* __restrict__ w_ada, const float* __restrict__ b_ada, float* __restrict__ MOD, int G, int c) {
;     ...
; #pragma unroll 16
;             for (int k = 0; k < 256; ++k) {
;                 const float wv = w[(size_t)k * 6 * D];
; #pragma unroll
;                 for (int b = 0; b < NB; ++b) acc[b] += cond[b * D + kp * 256 + k] * wv;
;             }
	v_pk_fma_f32 v[16:17], v[132:133], v[164:165], v[16:17] op_sel_hi:[0,1,1]
	v_pk_fma_f32 v[14:15], v[132:133], v[166:167], v[14:15] op_sel_hi:[0,1,1]
	v_pk_fma_f32 v[12:13], v[132:133], v[168:169], v[12:13] op_sel_hi:[0,1,1]
	v_pk_fma_f32 v[10:11], v[132:133], v[170:171], v[10:11] op_sel_hi:[0,1,1]
	global_load_dword v132, v[196:197], off
	v_lshl_add_u64 v[196:197], v[196:197], 0, s[16:17]
	ds_read2st64_b32 v[164:165], v198 offset0:0 offset1:16
	ds_read2st64_b32 v[166:167], v198 offset0:32 offset1:48
	ds_read2st64_b32 v[168:169], v198 offset0:64 offset1:80
	ds_read2st64_b32 v[170:171], v198 offset0:96 offset1:112
	v_add_u32_e32 v198, 4, v198
	s_waitcnt vmcnt(31) lgkmcnt(12)
	v_pk_fma_f32 v[16:17], v[134:135], v[172:173], v[16:17] op_sel_hi:[0,1,1]
	v_pk_fma_f32 v[14:15], v[134:135], v[174:175], v[14:15] op_sel_hi:[0,1,1]
	v_pk_fma_f32 v[12:13], v[134:135], v[176:177], v[12:13] op_sel_hi:[0,1,1]
	v_pk_fma_f32 v[10:11], v[134:135], v[178:179], v[10:11] op_sel_hi:[0,1,1]
	global_load_dword v134, v[196:197], off
	v_lshl_add_u64 v[196:197], v[196:197], 0, s[16:17]
	ds_read2st64_b32 v[172:173], v198 offset0:0 offset1:16
	ds_read2st64_b32 v[174:175], v198 offset0:32 offset1:48
	ds_read2st64_b32 v[176:177], v198 offset0:64 offset1:80
	ds_read2st64_b32 v[178:179], v198 offset0:96 offset1:112
	v_add_u32_e32 v198, 4, v198
	s_waitcnt vmcnt(31) lgkmcnt(12)
	v_pk_fma_f32 v[16:17], v[136:137], v[180:181], v[16:17] op_sel_hi:[0,1,1]
	v_pk_fma_f32 v[14:15], v[136:137], v[182:183], v[14:15] op_sel_hi:[0,1,1]
	v_pk_fma_f32 v[12:13], v[136:137], v[184:185], v[12:13] op_sel_hi:[0,1,1]
	v_pk_fma_f32 v[10:11], v[136:137], v[186:187], v[10:11] op_sel_hi:[0,1,1]
	global_load_dword v136, v[196:197], off
	v_lshl_add_u64 v[196:197], v[196:197], 0, s[16:17]
	ds_read2st64_b32 v[180:181], v198 offset0:0 offset1:16
	ds_read2st64_b32 v[182:183], v198 offset0:32 offset1:48
	ds_read2st64_b32 v[184:185], v198 offset0:64 offset1:80
	ds_read2st64_b32 v[186:187], v198 offset0:96 offset1:112
	v_add_u32_e32 v198, 4, v198
	s_waitcnt vmcnt(31) lgkmcnt(12)
	v_pk_fma_f32 v[16:17], v[138:139], v[188:189], v[16:17] op_sel_hi:[0,1,1]
	v_pk_fma_f32 v[14:15], v[138:139], v[190:191], v[14:15] op_sel_hi:[0,1,1]
	v_pk_fma_f32 v[12:13], v[138:139], v[192:193], v[12:13] op_sel_hi:[0,1,1]
	v_pk_fma_f32 v[10:11], v[138:139], v[194:195], v[10:11] op_sel_hi:[0,1,1]
	global_load_dword v138, v[196:197], off
	v_lshl_add_u64 v[196:197], v[196:197], 0, s[16:17]
	ds_read2st64_b32 v[188:189], v198 offset0:0 offset1:16
	ds_read2st64_b32 v[190:191], v198 offset0:32 offset1:48
	ds_read2st64_b32 v[192:193], v198 offset0:64 offset1:80
	ds_read2st64_b32 v[194:195], v198 offset0:96 offset1:112
	v_add_u32_e32 v198, 4, v198
	s_waitcnt vmcnt(31) lgkmcnt(12)
	v_pk_fma_f32 v[16:17], v[140:141], v[164:165], v[16:17] op_sel_hi:[0,1,1]
	v_pk_fma_f32 v[14:15], v[140:141], v[166:167], v[14:15] op_sel_hi:[0,1,1]
	v_pk_fma_f32 v[12:13], v[140:141], v[168:169], v[12:13] op_sel_hi:[0,1,1]
	v_pk_fma_f32 v[10:11], v[140:141], v[170:171], v[10:11] op_sel_hi:[0,1,1]
	global_load_dword v140, v[196:197], off
	v_lshl_add_u64 v[196:197], v[196:197], 0, s[16:17]
	ds_read2st64_b32 v[164:165], v198 offset0:0 offset1:16
	ds_read2st64_b32 v[166:167], v198 offset0:32 offset1:48
	ds_read2st64_b32 v[168:169], v198 offset0:64 offset1:80
	ds_read2st64_b32 v[170:171], v198 offset0:96 offset1:112
	v_add_u32_e32 v198, 4, v198
	s_waitcnt vmcnt(31) lgkmcnt(12)
	v_pk_fma_f32 v[16:17], v[142:143], v[172:173], v[16:17] op_sel_hi:[0,1,1]
	v_pk_fma_f32 v[14:15], v[142:143], v[174:175], v[14:15] op_sel_hi:[0,1,1]
	v_pk_fma_f32 v[12:13], v[142:143], v[176:177], v[12:13] op_sel_hi:[0,1,1]
	v_pk_fma_f32 v[10:11], v[142:143], v[178:179], v[10:11] op_sel_hi:[0,1,1]
	global_load_dword v142, v[196:197], off
	v_lshl_add_u64 v[196:197], v[196:197], 0, s[16:17]
	ds_read2st64_b32 v[172:173], v198 offset0:0 offset1:16
	ds_read2st64_b32 v[174:175], v198 offset0:32 offset1:48
	ds_read2st64_b32 v[176:177], v198 offset0:64 offset1:80
	ds_read2st64_b32 v[178:179], v198 offset0:96 offset1:112
	v_add_u32_e32 v198, 4, v198
	s_waitcnt vmcnt(31) lgkmcnt(12)
	v_pk_fma_f32 v[16:17], v[144:145], v[180:181], v[16:17] op_sel_hi:[0,1,1]
	v_pk_fma_f32 v[14:15], v[144:145], v[182:183], v[14:15] op_sel_hi:[0,1,1]
	v_pk_fma_f32 v[12:13], v[144:145], v[184:185], v[12:13] op_sel_hi:[0,1,1]
	v_pk_fma_f32 v[10:11], v[144:145], v[186:187], v[10:11] op_sel_hi:[0,1,1]
	global_load_dword v144, v[196:197], off
	v_lshl_add_u64 v[196:197], v[196:197], 0, s[16:17]
	ds_read2st64_b32 v[180:181], v198 offset0:0 offset1:16
	ds_read2st64_b32 v[182:183], v198 offset0:32 offset1:48
	ds_read2st64_b32 v[184:185], v198 offset0:64 offset1:80
	ds_read2st64_b32 v[186:187], v198 offset0:96 offset1:112
	v_add_u32_e32 v198, 4, v198
	s_waitcnt vmcnt(31) lgkmcnt(12)
	v_pk_fma_f32 v[16:17], v[146:147], v[188:189], v[16:17] op_sel_hi:[0,1,1]
	v_pk_fma_f32 v[14:15], v[146:147], v[190:191], v[14:15] op_sel_hi:[0,1,1]
	v_pk_fma_f32 v[12:13], v[146:147], v[192:193], v[12:13] op_sel_hi:[0,1,1]
	v_pk_fma_f32 v[10:11], v[146:147], v[194:195], v[10:11] op_sel_hi:[0,1,1]
	global_load_dword v146, v[196:197], off
	v_lshl_add_u64 v[196:197], v[196:197], 0, s[16:17]
	ds_read2st64_b32 v[188:189], v198 offset0:0 offset1:16
	ds_read2st64_b32 v[190:191], v198 offset0:32 offset1:48
	ds_read2st64_b32 v[192:193], v198 offset0:64 offset1:80
	ds_read2st64_b32 v[194:195], v198 offset0:96 offset1:112
	v_add_u32_e32 v198, 4, v198
	s_waitcnt vmcnt(31) lgkmcnt(12)
; __device__ __forceinline__ void ada_phase(LAS unsigned char* lds, const float* __restrict__ cin, const float* __restrict__ w_ada, const float* __restrict__ b_ada, float* __restrict__ MOD, int G, int c) {
;     ...
; #pragma unroll 16
;             for (int k = 0; k < 256; ++k) {
;                 const float wv = w[(size_t)k * 6 * D];
; #pragma unroll
;                 for (int b = 0; b < NB; ++b) acc[b] += cond[b * D + kp * 256 + k] * wv;
;             }
; #pragma unroll
;             for (int b = 0; b < NB; ++b) part[(kp * 96 + cl) * 8 + b] = acc[b];
	v_pk_fma_f32 v[16:17], v[148:149], v[164:165], v[16:17] op_sel_hi:[0,1,1]
	v_pk_fma_f32 v[14:15], v[148:149], v[166:167], v[14:15] op_sel_hi:[0,1,1]
	v_pk_fma_f32 v[12:13], v[148:149], v[168:169], v[12:13] op_sel_hi:[0,1,1]
	v_pk_fma_f32 v[10:11], v[148:149], v[170:171], v[10:11] op_sel_hi:[0,1,1]
	global_load_dword v148, v[196:197], off
	v_lshl_add_u64 v[196:197], v[196:197], 0, s[16:17]
	ds_read2st64_b32 v[164:165], v198 offset0:0 offset1:16
	ds_read2st64_b32 v[166:167], v198 offset0:32 offset1:48
	ds_read2st64_b32 v[168:169], v198 offset0:64 offset1:80
	ds_read2st64_b32 v[170:171], v198 offset0:96 offset1:112
	v_add_u32_e32 v198, 4, v198
	s_waitcnt vmcnt(31) lgkmcnt(12)
	v_pk_fma_f32 v[16:17], v[150:151], v[172:173], v[16:17] op_sel_hi:[0,1,1]
	v_pk_fma_f32 v[14:15], v[150:151], v[174:175], v[14:15] op_sel_hi:[0,1,1]
	v_pk_fma_f32 v[12:13], v[150:151], v[176:177], v[12:13] op_sel_hi:[0,1,1]
	v_pk_fma_f32 v[10:11], v[150:151], v[178:179], v[10:11] op_sel_hi:[0,1,1]
	global_load_dword v150, v[196:197], off
	v_lshl_add_u64 v[196:197], v[196:197], 0, s[16:17]
	ds_read2st64_b32 v[172:173], v198 offset0:0 offset1:16
	ds_read2st64_b32 v[174:175], v198 offset0:32 offset1:48
	ds_read2st64_b32 v[176:177], v198 offset0:64 offset1:80
	ds_read2st64_b32 v[178:179], v198 offset0:96 offset1:112
	v_add_u32_e32 v198, 4, v198
	s_waitcnt vmcnt(31) lgkmcnt(12)
	v_pk_fma_f32 v[16:17], v[152:153], v[180:181], v[16:17] op_sel_hi:[0,1,1]
	v_pk_fma_f32 v[14:15], v[152:153], v[182:183], v[14:15] op_sel_hi:[0,1,1]
	v_pk_fma_f32 v[12:13], v[152:153], v[184:185], v[12:13] op_sel_hi:[0,1,1]
	v_pk_fma_f32 v[10:11], v[152:153], v[186:187], v[10:11] op_sel_hi:[0,1,1]
	global_load_dword v152, v[196:197], off
	v_lshl_add_u64 v[196:197], v[196:197], 0, s[16:17]
	ds_read2st64_b32 v[180:181], v198 offset0:0 offset1:16
	ds_read2st64_b32 v[182:183], v198 offset0:32 offset1:48
	ds_read2st64_b32 v[184:185], v198 offset0:64 offset1:80
	ds_read2st64_b32 v[186:187], v198 offset0:96 offset1:112
	v_add_u32_e32 v198, 4, v198
	s_waitcnt vmcnt(31) lgkmcnt(12)
	v_pk_fma_f32 v[16:17], v[154:155], v[188:189], v[16:17] op_sel_hi:[0,1,1]
	v_pk_fma_f32 v[14:15], v[154:155], v[190:191], v[14:15] op_sel_hi:[0,1,1]
	v_pk_fma_f32 v[12:13], v[154:155], v[192:193], v[12:13] op_sel_hi:[0,1,1]
	v_pk_fma_f32 v[10:11], v[154:155], v[194:195], v[10:11] op_sel_hi:[0,1,1]
	global_load_dword v154, v[196:197], off
	v_lshl_add_u64 v[196:197], v[196:197], 0, s[16:17]
	ds_read2st64_b32 v[188:189], v198 offset0:0 offset1:16
	ds_read2st64_b32 v[190:191], v198 offset0:32 offset1:48
	ds_read2st64_b32 v[192:193], v198 offset0:64 offset1:80
	ds_read2st64_b32 v[194:195], v198 offset0:96 offset1:112
	v_add_u32_e32 v198, 4, v198
	s_waitcnt vmcnt(31) lgkmcnt(12)
	v_pk_fma_f32 v[16:17], v[156:157], v[164:165], v[16:17] op_sel_hi:[0,1,1]
	v_pk_fma_f32 v[14:15], v[156:157], v[166:167], v[14:15] op_sel_hi:[0,1,1]
	v_pk_fma_f32 v[12:13], v[156:157], v[168:169], v[12:13] op_sel_hi:[0,1,1]
	v_pk_fma_f32 v[10:11], v[156:157], v[170:171], v[10:11] op_sel_hi:[0,1,1]
	global_load_dword v156, v[196:197], off
	v_lshl_add_u64 v[196:197], v[196:197], 0, s[16:17]
	ds_read2st64_b32 v[164:165], v198 offset0:0 offset1:16
	ds_read2st64_b32 v[166:167], v198 offset0:32 offset1:48
	ds_read2st64_b32 v[168:169], v198 offset0:64 offset1:80
	ds_read2st64_b32 v[170:171], v198 offset0:96 offset1:112
	v_add_u32_e32 v198, 4, v198
	s_waitcnt vmcnt(31) lgkmcnt(12)
	v_pk_fma_f32 v[16:17], v[158:159], v[172:173], v[16:17] op_sel_hi:[0,1,1]
	v_pk_fma_f32 v[14:15], v[158:159], v[174:175], v[14:15] op_sel_hi:[0,1,1]
	v_pk_fma_f32 v[12:13], v[158:159], v[176:177], v[12:13] op_sel_hi:[0,1,1]
	v_pk_fma_f32 v[10:11], v[158:159], v[178:179], v[10:11] op_sel_hi:[0,1,1]
	global_load_dword v158, v[196:197], off
	v_lshl_add_u64 v[196:197], v[196:197], 0, s[16:17]
	ds_read2st64_b32 v[172:173], v198 offset0:0 offset1:16
	ds_read2st64_b32 v[174:175], v198 offset0:32 offset1:48
	ds_read2st64_b32 v[176:177], v198 offset0:64 offset1:80
	ds_read2st64_b32 v[178:179], v198 offset0:96 offset1:112
	v_add_u32_e32 v198, 4, v198
	s_waitcnt vmcnt(31) lgkmcnt(12)
	v_pk_fma_f32 v[16:17], v[160:161], v[180:181], v[16:17] op_sel_hi:[0,1,1]
	v_pk_fma_f32 v[14:15], v[160:161], v[182:183], v[14:15] op_sel_hi:[0,1,1]
	v_pk_fma_f32 v[12:13], v[160:161], v[184:185], v[12:13] op_sel_hi:[0,1,1]
	v_pk_fma_f32 v[10:11], v[160:161], v[186:187], v[10:11] op_sel_hi:[0,1,1]
	global_load_dword v160, v[196:197], off
	v_lshl_add_u64 v[196:197], v[196:197], 0, s[16:17]
	ds_read2st64_b32 v[180:181], v198 offset0:0 offset1:16
	ds_read2st64_b32 v[182:183], v198 offset0:32 offset1:48
	ds_read2st64_b32 v[184:185], v198 offset0:64 offset1:80
	ds_read2st64_b32 v[186:187], v198 offset0:96 offset1:112
	v_add_u32_e32 v198, 4, v198
	s_waitcnt vmcnt(31) lgkmcnt(12)
	v_pk_fma_f32 v[16:17], v[162:163], v[188:189], v[16:17] op_sel_hi:[0,1,1]
	v_pk_fma_f32 v[14:15], v[162:163], v[190:191], v[14:15] op_sel_hi:[0,1,1]
	v_pk_fma_f32 v[12:13], v[162:163], v[192:193], v[12:13] op_sel_hi:[0,1,1]
	v_pk_fma_f32 v[10:11], v[162:163], v[194:195], v[10:11] op_sel_hi:[0,1,1]
	global_load_dword v162, v[196:197], off
	v_lshl_add_u64 v[196:197], v[196:197], 0, s[16:17]
	s_add_i32 s10, s10, -1
	s_cmp_lt_i32 s10, 0
	s_cbranch_scc0 .Lada_blk
	s_waitcnt vmcnt(0) lgkmcnt(0)
	v_add_u32_e32 v8, 0x8000, v40
	ds_write2_b32 v8, v16, v17 offset1:1
	v_add_u32_e32 v8, 0x8008, v40
	ds_write2_b32 v8, v14, v15 offset1:1
	v_add_u32_e32 v8, 0x8010, v40
	ds_write2_b32 v8, v12, v13 offset1:1
	v_add_u32_e32 v8, 0x8018, v40
	ds_write2_b32 v8, v10, v11 offset1:1
